# combo4 + Gray-code MFMA order in the four fp8 GEMM loops (consecutive MFMAs share one fragment operand; P8 guards follow their MFMA)
# speedup vs baseline: 1.0055x; 1.0055x over previous
.LBB0_200:
	s_add_u32 s72, s42, 0xfff80000
	s_addc_u32 s73, s43, -1
	s_mov_b32 m0, s57
	s_nop 0
	global_load_lds_dwordx4 v160, s[72:73]
	s_mov_b32 m0, s58
	s_nop 0
	global_load_lds_dwordx4 v164, s[72:73]
	ds_read_b128 v[16:19], v186
	ds_read_b128 v[20:23], v187
	ds_read_b128 v[24:27], v188
	ds_read_b128 v[28:31], v189
	ds_read_b128 v[0:3], v190
	ds_read_b128 v[4:7], v191
	ds_read_b128 v[8:11], v192
	ds_read_b128 v[12:15], v193
	s_add_u32 s44, s42, 0xfff80080
	s_addc_u32 s45, s43, -1
	s_cmp_eq_u32 s68, 28
	s_cselect_b32 s47, s31, s45
	s_cselect_b32 s46, s35, s44
	s_cselect_b32 s45, s29, s67
	s_cselect_b32 s44, s39, s66
	s_add_i32 m0, s27, 0xc000
	ds_read_b128 v[178:181], v218
	ds_read_b128 v[182:185], v218 offset:1024
	ds_read_b128 v[222:225], v218 offset:2048
	ds_read_b128 v[226:229], v218 offset:3072
	ds_read_b128 v[230:233], v218 offset:4096
	ds_read_b128 v[234:237], v218 offset:5120
	ds_read_b128 v[238:241], v218 offset:6144
	ds_read_b128 v[242:245], v218 offset:7168
	global_load_lds_dwordx4 v172, s[42:43]
	s_add_i32 m0, s27, 0xe000
	s_nop 0
	global_load_lds_dwordx4 v174, s[42:43]
	s_waitcnt vmcnt(8)
	s_waitcnt lgkmcnt(0)
	s_barrier
	s_setprio 1
	s_waitcnt lgkmcnt(0)
	v_mfma_f32_16x16x128_f8f6f4 v[156:159], v[16:23], v[178:185], v[156:159]
	v_mfma_f32_16x16x128_f8f6f4 v[152:155], v[24:31], v[178:185], v[152:155]
	v_mfma_f32_16x16x128_f8f6f4 v[144:147], v[24:31], v[222:229], v[144:147]
	v_mfma_f32_16x16x128_f8f6f4 v[148:151], v[16:23], v[222:229], v[148:151]
	v_mfma_f32_16x16x128_f8f6f4 v[140:143], v[16:23], v[230:237], v[140:143]
	v_mfma_f32_16x16x128_f8f6f4 v[136:139], v[24:31], v[230:237], v[136:139]
	v_mfma_f32_16x16x128_f8f6f4 v[128:131], v[24:31], v[238:245], v[128:131]
	v_mfma_f32_16x16x128_f8f6f4 v[132:135], v[16:23], v[238:245], v[132:135]
	s_setprio 0
	s_setprio 1
	v_mfma_f32_16x16x128_f8f6f4 v[100:103], v[0:7], v[238:245], v[100:103]
	v_mfma_f32_16x16x128_f8f6f4 v[96:99], v[8:15], v[238:245], v[96:99]
	v_mfma_f32_16x16x128_f8f6f4 v[104:107], v[8:15], v[230:237], v[104:107]
	v_mfma_f32_16x16x128_f8f6f4 v[108:111], v[0:7], v[230:237], v[108:111]
	v_mfma_f32_16x16x128_f8f6f4 v[116:119], v[0:7], v[222:229], v[116:119]
	v_mfma_f32_16x16x128_f8f6f4 v[112:115], v[8:15], v[222:229], v[112:115]
	v_mfma_f32_16x16x128_f8f6f4 v[120:123], v[8:15], v[178:185], v[120:123]
	v_mfma_f32_16x16x128_f8f6f4 v[124:127], v[0:7], v[178:185], v[124:127]
	s_setprio 0
	s_barrier
	s_mov_b32 m0, s33
	v_lshl_add_u64 v[178:179], s[44:45], 0, v[162:163]
	s_add_u32 s70, s44, 0x80000
	ds_read_b128 v[222:225], v218 offset:16384
	ds_read_b128 v[226:229], v218 offset:17408
	ds_read_b128 v[230:233], v218 offset:18432
	ds_read_b128 v[234:237], v218 offset:19456
	ds_read_b128 v[238:241], v218 offset:20480
	ds_read_b128 v[242:245], v218 offset:21504
	ds_read_b128 v[246:249], v218 offset:22528
	ds_read_b128 v[250:253], v218 offset:23552
	global_load_lds_dwordx4 v[178:179], off
	v_lshl_add_u64 v[180:181], s[44:45], 0, v[166:167]
	s_mov_b32 m0, s48
	s_addc_u32 s71, s45, 0
	global_load_lds_dwordx4 v[180:181], off
	s_mov_b32 m0, s49
	s_nop 0
	global_load_lds_dwordx4 v162, s[70:71]
	s_mov_b32 m0, s50
	s_nop 0
	global_load_lds_dwordx4 v166, s[70:71]
	s_waitcnt vmcnt(6)
	s_waitcnt lgkmcnt(0)
	s_barrier
	s_setprio 1
	s_waitcnt lgkmcnt(0)
	v_mfma_f32_16x16x128_f8f6f4 v[92:95], v[16:23], v[222:229], v[92:95]
	v_mfma_f32_16x16x128_f8f6f4 v[88:91], v[24:31], v[222:229], v[88:91]
	v_mfma_f32_16x16x128_f8f6f4 v[80:83], v[24:31], v[230:237], v[80:83]
	v_mfma_f32_16x16x128_f8f6f4 v[84:87], v[16:23], v[230:237], v[84:87]
	v_mfma_f32_16x16x128_f8f6f4 v[76:79], v[16:23], v[238:245], v[76:79]
	v_mfma_f32_16x16x128_f8f6f4 v[72:75], v[24:31], v[238:245], v[72:75]
	v_mfma_f32_16x16x128_f8f6f4 v[64:67], v[24:31], v[246:253], v[64:67]
	v_mfma_f32_16x16x128_f8f6f4 v[68:71], v[16:23], v[246:253], v[68:71]
	s_setprio 0
	s_setprio 1
	v_mfma_f32_16x16x128_f8f6f4 v[36:39], v[0:7], v[246:253], v[36:39]
	v_mfma_f32_16x16x128_f8f6f4 v[32:35], v[8:15], v[246:253], v[32:35]
	v_mfma_f32_16x16x128_f8f6f4 v[40:43], v[8:15], v[238:245], v[40:43]
	v_mfma_f32_16x16x128_f8f6f4 v[44:47], v[0:7], v[238:245], v[44:47]
	v_mfma_f32_16x16x128_f8f6f4 v[52:55], v[0:7], v[230:237], v[52:55]
	v_mfma_f32_16x16x128_f8f6f4 v[48:51], v[8:15], v[230:237], v[48:51]
	v_mfma_f32_16x16x128_f8f6f4 v[56:59], v[8:15], v[222:229], v[56:59]
	v_mfma_f32_16x16x128_f8f6f4 v[60:63], v[0:7], v[222:229], v[60:63]
	s_setprio 0
	s_barrier
	s_mov_b32 m0, s27
	s_nop 0
	global_load_lds_dwordx4 v160, s[46:47]
	s_mov_b32 m0, s51
	s_nop 0
	global_load_lds_dwordx4 v164, s[46:47]
	ds_read_b128 v[0:3], v194
	ds_read_b128 v[4:7], v195
	ds_read_b128 v[8:11], v196
	ds_read_b128 v[12:15], v197
	ds_read_b128 v[16:19], v198
	ds_read_b128 v[20:23], v199
	ds_read_b128 v[24:27], v200
	ds_read_b128 v[28:31], v201
	s_add_u32 s46, s46, 0x80000
	s_addc_u32 s47, s47, 0
	s_mov_b32 m0, s52
	ds_read_b128 v[222:225], v218 offset:32768
	ds_read_b128 v[226:229], v218 offset:33792
	ds_read_b128 v[230:233], v218 offset:34816
	ds_read_b128 v[234:237], v218 offset:35840
	ds_read_b128 v[238:241], v218 offset:36864
	ds_read_b128 v[242:245], v218 offset:37888
	ds_read_b128 v[246:249], v218 offset:38912
	ds_read_b128 v[250:253], v218 offset:39936
	global_load_lds_dwordx4 v160, s[46:47]
	s_mov_b32 m0, s53
	s_nop 0
	global_load_lds_dwordx4 v164, s[46:47]
	s_waitcnt vmcnt(8)
	s_waitcnt lgkmcnt(0)
	s_barrier
	s_setprio 1
	s_waitcnt lgkmcnt(0)
	v_mfma_f32_16x16x128_f8f6f4 v[156:159], v[0:7], v[222:229], v[156:159]
	v_mfma_f32_16x16x128_f8f6f4 v[152:155], v[8:15], v[222:229], v[152:155]
	v_mfma_f32_16x16x128_f8f6f4 v[144:147], v[8:15], v[230:237], v[144:147]
	v_mfma_f32_16x16x128_f8f6f4 v[148:151], v[0:7], v[230:237], v[148:151]
	v_mfma_f32_16x16x128_f8f6f4 v[140:143], v[0:7], v[238:245], v[140:143]
	v_mfma_f32_16x16x128_f8f6f4 v[136:139], v[8:15], v[238:245], v[136:139]
	v_mfma_f32_16x16x128_f8f6f4 v[128:131], v[8:15], v[246:253], v[128:131]
	v_mfma_f32_16x16x128_f8f6f4 v[132:135], v[0:7], v[246:253], v[132:135]
	s_setprio 0
	s_setprio 1
	v_mfma_f32_16x16x128_f8f6f4 v[100:103], v[16:23], v[246:253], v[100:103]
	v_mfma_f32_16x16x128_f8f6f4 v[96:99], v[24:31], v[246:253], v[96:99]
	v_mfma_f32_16x16x128_f8f6f4 v[104:107], v[24:31], v[238:245], v[104:107]
	v_mfma_f32_16x16x128_f8f6f4 v[108:111], v[16:23], v[238:245], v[108:111]
	v_mfma_f32_16x16x128_f8f6f4 v[116:119], v[16:23], v[230:237], v[116:119]
	v_mfma_f32_16x16x128_f8f6f4 v[112:115], v[24:31], v[230:237], v[112:115]
	v_mfma_f32_16x16x128_f8f6f4 v[120:123], v[24:31], v[222:229], v[120:123]
	v_mfma_f32_16x16x128_f8f6f4 v[124:127], v[16:23], v[222:229], v[124:127]
	s_setprio 0
	s_barrier
	s_mov_b32 m0, s55
	v_lshl_add_u64 v[176:177], v[178:179], 0, s[20:21]
	s_add_u32 s44, s44, 0x80080
	ds_read_b128 v[222:225], v218 offset:49152
	ds_read_b128 v[226:229], v218 offset:50176
	ds_read_b128 v[230:233], v218 offset:51200
	ds_read_b128 v[234:237], v218 offset:52224
	ds_read_b128 v[238:241], v218 offset:53248
	ds_read_b128 v[242:245], v218 offset:54272
	ds_read_b128 v[246:249], v218 offset:55296
	ds_read_b128 v[250:253], v218 offset:56320
	global_load_lds_dwordx4 v[176:177], off
	v_lshl_add_u64 v[176:177], v[180:181], 0, s[20:21]
	s_mov_b32 m0, s56
	s_addc_u32 s45, s45, 0
	global_load_lds_dwordx4 v[176:177], off
	s_mov_b32 m0, s59
	s_nop 0
	global_load_lds_dwordx4 v162, s[44:45]
	s_mov_b32 m0, s60
	s_nop 0
	global_load_lds_dwordx4 v166, s[44:45]
	s_waitcnt vmcnt(6)
	s_waitcnt lgkmcnt(0)
	s_barrier
	s_setprio 1
	s_waitcnt lgkmcnt(0)
	v_mfma_f32_16x16x128_f8f6f4 v[92:95], v[0:7], v[222:229], v[92:95]
	v_mfma_f32_16x16x128_f8f6f4 v[88:91], v[8:15], v[222:229], v[88:91]
	v_mfma_f32_16x16x128_f8f6f4 v[80:83], v[8:15], v[230:237], v[80:83]
	v_mfma_f32_16x16x128_f8f6f4 v[84:87], v[0:7], v[230:237], v[84:87]
	v_mfma_f32_16x16x128_f8f6f4 v[76:79], v[0:7], v[238:245], v[76:79]
	v_mfma_f32_16x16x128_f8f6f4 v[72:75], v[8:15], v[238:245], v[72:75]
	v_mfma_f32_16x16x128_f8f6f4 v[64:67], v[8:15], v[246:253], v[64:67]
	v_mfma_f32_16x16x128_f8f6f4 v[68:71], v[0:7], v[246:253], v[68:71]
	s_setprio 0
	s_setprio 1
	v_mfma_f32_16x16x128_f8f6f4 v[36:39], v[16:23], v[246:253], v[36:39]
	v_mfma_f32_16x16x128_f8f6f4 v[32:35], v[24:31], v[246:253], v[32:35]
	v_mfma_f32_16x16x128_f8f6f4 v[40:43], v[24:31], v[238:245], v[40:43]
	v_mfma_f32_16x16x128_f8f6f4 v[44:47], v[16:23], v[238:245], v[44:47]
	v_mfma_f32_16x16x128_f8f6f4 v[52:55], v[16:23], v[230:237], v[52:55]
	v_mfma_f32_16x16x128_f8f6f4 v[48:51], v[24:31], v[230:237], v[48:51]
	v_mfma_f32_16x16x128_f8f6f4 v[56:59], v[24:31], v[222:229], v[56:59]
	v_mfma_f32_16x16x128_f8f6f4 v[60:63], v[16:23], v[222:229], v[60:63]
	s_setprio 0
	s_barrier
	s_add_i32 s68, s68, 2
	s_add_u32 s42, s42, 0x100
	s_addc_u32 s43, s43, 0
	s_add_u32 s66, s66, 0x100
	s_addc_u32 s67, s67, 0
	s_cmp_gt_u32 s68, 29
	s_cbranch_scc0 .LBB0_200
	s_nop 15
	s_nop 15
	s_and_b64 vcc, exec, s[22:23]
	s_cbranch_vccz .LBB0_203
	s_barrier

.LBB0_562:
	s_add_u32 s72, s30, 0xfff80000
	s_addc_u32 s73, s31, -1
	s_mov_b32 m0, s49
	s_nop 0
	global_load_lds_dwordx4 v160, s[72:73]
	s_mov_b32 m0, s50
	s_nop 0
	global_load_lds_dwordx4 v162, s[72:73]
	ds_read_b128 v[16:19], v181
	ds_read_b128 v[20:23], v182
	ds_read_b128 v[24:27], v183
	ds_read_b128 v[28:31], v184
	ds_read_b128 v[0:3], v185
	ds_read_b128 v[4:7], v186
	ds_read_b128 v[8:11], v187
	ds_read_b128 v[12:15], v188
	s_add_u32 s34, s30, 0xfff80080
	s_addc_u32 s35, s31, -1
	s_cmp_eq_u32 s59, 28
	s_cselect_b32 s37, s23, s35
	s_cselect_b32 s36, s55, s34
	s_cselect_b32 s35, s21, s58
	s_cselect_b32 s34, s56, s57
	s_add_i32 m0, s29, 0xc000
	ds_read_b128 v[172:175], v198
	ds_read_b128 v[176:179], v198 offset:1024
	ds_read_b128 v[200:203], v198 offset:2048
	ds_read_b128 v[204:207], v198 offset:3072
	ds_read_b128 v[208:211], v198 offset:4096
	ds_read_b128 v[212:215], v198 offset:5120
	ds_read_b128 v[216:219], v198 offset:6144
	ds_read_b128 v[220:223], v198 offset:7168
	global_load_lds_dwordx4 v164, s[30:31]
	s_add_i32 m0, s29, 0xe000
	s_nop 0
	global_load_lds_dwordx4 v166, s[30:31]
	s_waitcnt vmcnt(8)
	s_waitcnt lgkmcnt(0)
	s_barrier
	s_setprio 1
	s_waitcnt lgkmcnt(0)
	v_mfma_f32_16x16x128_f8f6f4 v[156:159], v[16:23], v[172:179], v[156:159]
	v_mfma_f32_16x16x128_f8f6f4 v[152:155], v[24:31], v[172:179], v[152:155]
	v_mfma_f32_16x16x128_f8f6f4 v[144:147], v[24:31], v[200:207], v[144:147]
	v_mfma_f32_16x16x128_f8f6f4 v[148:151], v[16:23], v[200:207], v[148:151]
	v_mfma_f32_16x16x128_f8f6f4 v[124:127], v[16:23], v[208:215], v[124:127]
	v_mfma_f32_16x16x128_f8f6f4 v[120:123], v[24:31], v[208:215], v[120:123]
	v_mfma_f32_16x16x128_f8f6f4 v[112:115], v[24:31], v[216:223], v[112:115]
	v_mfma_f32_16x16x128_f8f6f4 v[116:119], v[16:23], v[216:223], v[116:119]
	s_setprio 0
	s_setprio 1
	v_mfma_f32_16x16x128_f8f6f4 v[100:103], v[0:7], v[216:223], v[100:103]
	v_mfma_f32_16x16x128_f8f6f4 v[96:99], v[8:15], v[216:223], v[96:99]
	v_mfma_f32_16x16x128_f8f6f4 v[104:107], v[8:15], v[208:215], v[104:107]
	v_mfma_f32_16x16x128_f8f6f4 v[108:111], v[0:7], v[208:215], v[108:111]
	v_mfma_f32_16x16x128_f8f6f4 v[132:135], v[0:7], v[200:207], v[132:135]
	v_mfma_f32_16x16x128_f8f6f4 v[128:131], v[8:15], v[200:207], v[128:131]
	v_mfma_f32_16x16x128_f8f6f4 v[136:139], v[8:15], v[172:179], v[136:139]
	v_mfma_f32_16x16x128_f8f6f4 v[140:143], v[0:7], v[172:179], v[140:143]
	s_setprio 0
	s_barrier
	s_mov_b32 m0, s33
	v_lshl_add_u64 v[172:173], s[34:35], 0, v[160:161]
	s_add_u32 s60, s34, 0x80000
	ds_read_b128 v[200:203], v198 offset:16384
	ds_read_b128 v[204:207], v198 offset:17408
	ds_read_b128 v[208:211], v198 offset:18432
	ds_read_b128 v[212:215], v198 offset:19456
	ds_read_b128 v[216:219], v198 offset:20480
	ds_read_b128 v[220:223], v198 offset:21504
	ds_read_b128 v[224:227], v198 offset:22528
	ds_read_b128 v[228:231], v198 offset:23552
	global_load_lds_dwordx4 v[172:173], off
	v_lshl_add_u64 v[174:175], s[34:35], 0, v[162:163]
	s_mov_b32 m0, s38
	s_addc_u32 s61, s35, 0
	global_load_lds_dwordx4 v[174:175], off
	s_mov_b32 m0, s39
	s_nop 0
	global_load_lds_dwordx4 v160, s[60:61]
	s_mov_b32 m0, s40
	s_nop 0
	global_load_lds_dwordx4 v162, s[60:61]
	s_waitcnt vmcnt(6)
	s_waitcnt lgkmcnt(0)
	s_barrier
	s_setprio 1
	s_waitcnt lgkmcnt(0)
	v_mfma_f32_16x16x128_f8f6f4 v[92:95], v[16:23], v[200:207], v[92:95]
	v_mfma_f32_16x16x128_f8f6f4 v[88:91], v[24:31], v[200:207], v[88:91]
	v_mfma_f32_16x16x128_f8f6f4 v[80:83], v[24:31], v[208:215], v[80:83]
	v_mfma_f32_16x16x128_f8f6f4 v[84:87], v[16:23], v[208:215], v[84:87]
	v_mfma_f32_16x16x128_f8f6f4 v[60:63], v[16:23], v[216:223], v[60:63]
	v_mfma_f32_16x16x128_f8f6f4 v[56:59], v[24:31], v[216:223], v[56:59]
	v_mfma_f32_16x16x128_f8f6f4 v[48:51], v[24:31], v[224:231], v[48:51]
	v_mfma_f32_16x16x128_f8f6f4 v[52:55], v[16:23], v[224:231], v[52:55]
	s_setprio 0
	s_setprio 1
	v_mfma_f32_16x16x128_f8f6f4 v[36:39], v[0:7], v[224:231], v[36:39]
	v_mfma_f32_16x16x128_f8f6f4 v[32:35], v[8:15], v[224:231], v[32:35]
	v_mfma_f32_16x16x128_f8f6f4 v[40:43], v[8:15], v[216:223], v[40:43]
	v_mfma_f32_16x16x128_f8f6f4 v[44:47], v[0:7], v[216:223], v[44:47]
	v_mfma_f32_16x16x128_f8f6f4 v[68:71], v[0:7], v[208:215], v[68:71]
	v_mfma_f32_16x16x128_f8f6f4 v[64:67], v[8:15], v[208:215], v[64:67]
	v_mfma_f32_16x16x128_f8f6f4 v[72:75], v[8:15], v[200:207], v[72:75]
	v_mfma_f32_16x16x128_f8f6f4 v[76:79], v[0:7], v[200:207], v[76:79]
	s_setprio 0
	s_barrier
	s_mov_b32 m0, s29
	s_nop 0
	global_load_lds_dwordx4 v160, s[36:37]
	s_mov_b32 m0, s41
	s_nop 0
	global_load_lds_dwordx4 v162, s[36:37]
	ds_read_b128 v[0:3], v189
	ds_read_b128 v[4:7], v190
	ds_read_b128 v[8:11], v191
	ds_read_b128 v[12:15], v192
	ds_read_b128 v[16:19], v193
	ds_read_b128 v[20:23], v194
	ds_read_b128 v[24:27], v195
	ds_read_b128 v[28:31], v196
	s_add_u32 s36, s36, 0x80000
	s_addc_u32 s37, s37, 0
	s_mov_b32 m0, s42
	ds_read_b128 v[200:203], v198 offset:32768
	ds_read_b128 v[204:207], v198 offset:33792
	ds_read_b128 v[208:211], v198 offset:34816
	ds_read_b128 v[212:215], v198 offset:35840
	ds_read_b128 v[216:219], v198 offset:36864
	ds_read_b128 v[220:223], v198 offset:37888
	ds_read_b128 v[224:227], v198 offset:38912
	ds_read_b128 v[228:231], v198 offset:39936
	global_load_lds_dwordx4 v160, s[36:37]
	s_mov_b32 m0, s43
	s_nop 0
	global_load_lds_dwordx4 v162, s[36:37]
	s_waitcnt vmcnt(8)
	s_waitcnt lgkmcnt(0)
	s_barrier
	s_setprio 1
	s_waitcnt lgkmcnt(0)
	v_mfma_f32_16x16x128_f8f6f4 v[156:159], v[0:7], v[200:207], v[156:159]
	v_mfma_f32_16x16x128_f8f6f4 v[152:155], v[8:15], v[200:207], v[152:155]
	v_mfma_f32_16x16x128_f8f6f4 v[144:147], v[8:15], v[208:215], v[144:147]
	v_mfma_f32_16x16x128_f8f6f4 v[148:151], v[0:7], v[208:215], v[148:151]
	v_mfma_f32_16x16x128_f8f6f4 v[124:127], v[0:7], v[216:223], v[124:127]
	v_mfma_f32_16x16x128_f8f6f4 v[120:123], v[8:15], v[216:223], v[120:123]
	v_mfma_f32_16x16x128_f8f6f4 v[112:115], v[8:15], v[224:231], v[112:115]
	v_mfma_f32_16x16x128_f8f6f4 v[116:119], v[0:7], v[224:231], v[116:119]
	s_setprio 0
	s_setprio 1
	v_mfma_f32_16x16x128_f8f6f4 v[100:103], v[16:23], v[224:231], v[100:103]
	v_mfma_f32_16x16x128_f8f6f4 v[96:99], v[24:31], v[224:231], v[96:99]
	v_mfma_f32_16x16x128_f8f6f4 v[104:107], v[24:31], v[216:223], v[104:107]
	v_mfma_f32_16x16x128_f8f6f4 v[108:111], v[16:23], v[216:223], v[108:111]
	v_mfma_f32_16x16x128_f8f6f4 v[132:135], v[16:23], v[208:215], v[132:135]
	v_mfma_f32_16x16x128_f8f6f4 v[128:131], v[24:31], v[208:215], v[128:131]
	v_mfma_f32_16x16x128_f8f6f4 v[136:139], v[24:31], v[200:207], v[136:139]
	v_mfma_f32_16x16x128_f8f6f4 v[140:143], v[16:23], v[200:207], v[140:143]
	s_setprio 0
	s_barrier
	s_mov_b32 m0, s47
	v_lshl_add_u64 v[172:173], v[172:173], 0, s[14:15]
	s_add_u32 s34, s34, 0x80080
	ds_read_b128 v[200:203], v198 offset:49152
	ds_read_b128 v[204:207], v198 offset:50176
	ds_read_b128 v[208:211], v198 offset:51200
	ds_read_b128 v[212:215], v198 offset:52224
	ds_read_b128 v[216:219], v198 offset:53248
	ds_read_b128 v[220:223], v198 offset:54272
	ds_read_b128 v[224:227], v198 offset:55296
	ds_read_b128 v[228:231], v198 offset:56320
	global_load_lds_dwordx4 v[172:173], off
	v_lshl_add_u64 v[172:173], v[174:175], 0, s[14:15]
	s_mov_b32 m0, s48
	s_addc_u32 s35, s35, 0
	global_load_lds_dwordx4 v[172:173], off
	s_mov_b32 m0, s51
	s_nop 0
	global_load_lds_dwordx4 v160, s[34:35]
	s_mov_b32 m0, s52
	s_nop 0
	global_load_lds_dwordx4 v162, s[34:35]
	s_waitcnt vmcnt(6)
	s_waitcnt lgkmcnt(0)
	s_barrier
	s_setprio 1
	s_waitcnt lgkmcnt(0)
	v_mfma_f32_16x16x128_f8f6f4 v[92:95], v[0:7], v[200:207], v[92:95]
	v_mfma_f32_16x16x128_f8f6f4 v[88:91], v[8:15], v[200:207], v[88:91]
	v_mfma_f32_16x16x128_f8f6f4 v[80:83], v[8:15], v[208:215], v[80:83]
	v_mfma_f32_16x16x128_f8f6f4 v[84:87], v[0:7], v[208:215], v[84:87]
	v_mfma_f32_16x16x128_f8f6f4 v[60:63], v[0:7], v[216:223], v[60:63]
	v_mfma_f32_16x16x128_f8f6f4 v[56:59], v[8:15], v[216:223], v[56:59]
	v_mfma_f32_16x16x128_f8f6f4 v[48:51], v[8:15], v[224:231], v[48:51]
	v_mfma_f32_16x16x128_f8f6f4 v[52:55], v[0:7], v[224:231], v[52:55]
	s_setprio 0
	s_setprio 1
	v_mfma_f32_16x16x128_f8f6f4 v[36:39], v[16:23], v[224:231], v[36:39]
	v_mfma_f32_16x16x128_f8f6f4 v[32:35], v[24:31], v[224:231], v[32:35]
	v_mfma_f32_16x16x128_f8f6f4 v[40:43], v[24:31], v[216:223], v[40:43]
	v_mfma_f32_16x16x128_f8f6f4 v[44:47], v[16:23], v[216:223], v[44:47]
	v_mfma_f32_16x16x128_f8f6f4 v[68:71], v[16:23], v[208:215], v[68:71]
	v_mfma_f32_16x16x128_f8f6f4 v[64:67], v[24:31], v[208:215], v[64:67]
	v_mfma_f32_16x16x128_f8f6f4 v[72:75], v[24:31], v[200:207], v[72:75]
	v_mfma_f32_16x16x128_f8f6f4 v[76:79], v[16:23], v[200:207], v[76:79]
	s_setprio 0
	s_barrier
	s_add_i32 s59, s59, 2
	s_add_u32 s30, s30, 0x100
	s_addc_u32 s31, s31, 0
	s_add_u32 s57, s57, 0x100
	s_addc_u32 s58, s58, 0
	s_cmp_gt_u32 s59, 29
	s_cbranch_scc0 .LBB0_562
	s_nop 15
	s_nop 15
	s_and_b64 vcc, exec, s[16:17]
	s_cbranch_vccz .LBB0_565
	s_barrier

.Lp8s_0:
	s_bitcmp1_b32 s74, 1
	s_cbranch_scc0 .Lp8s_1
	v_mfma_f32_16x16x128_f8f6f4 v[152:155], v[24:31], v[180:187], v[152:155]
.Lp8s_1:
	s_bitcmp1_b32 s74, 5
	s_cbranch_scc0 .Lp8s_2
	v_mfma_f32_16x16x128_f8f6f4 v[136:139], v[24:31], v[208:215], v[136:139]
.Lp8s_2:
	s_bitcmp1_b32 s74, 4
	s_cbranch_scc0 .Lp8s_3
	v_mfma_f32_16x16x128_f8f6f4 v[140:143], v[16:23], v[208:215], v[140:143]
.Lp8s_3:
	s_bitcmp1_b32 s74, 8
	s_cbranch_scc0 .Lp8s_4
	v_mfma_f32_16x16x128_f8f6f4 v[124:127], v[16:23], v[216:223], v[124:127]
.Lp8s_4:
	s_bitcmp1_b32 s74, 9
	s_cbranch_scc0 .Lp8s_5
	v_mfma_f32_16x16x128_f8f6f4 v[120:123], v[24:31], v[216:223], v[120:123]
.Lp8s_5:
	s_bitcmp1_b32 s74, 13
	s_cbranch_scc0 .Lp8s_6
	v_mfma_f32_16x16x128_f8f6f4 v[104:107], v[24:31], v[224:231], v[104:107]
.Lp8s_6:
	s_bitcmp1_b32 s74, 12
	s_cbranch_scc0 .Lp8s_7
	v_mfma_f32_16x16x128_f8f6f4 v[108:111], v[16:23], v[224:231], v[108:111]
.Lp8s_7:
	s_setprio 0
	s_setprio 1
	s_bitcmp1_b32 s74, 14
	s_cbranch_scc0 .Lp8s_8
	v_mfma_f32_16x16x128_f8f6f4 v[100:103], v[0:7], v[224:231], v[100:103]
.Lp8s_8:
	s_bitcmp1_b32 s74, 15
	s_cbranch_scc0 .Lp8s_9
	v_mfma_f32_16x16x128_f8f6f4 v[96:99], v[8:15], v[224:231], v[96:99]
.Lp8s_9:
	s_bitcmp1_b32 s74, 11
	s_cbranch_scc0 .Lp8s_10
	v_mfma_f32_16x16x128_f8f6f4 v[112:115], v[8:15], v[216:223], v[112:115]
.Lp8s_10:
	s_bitcmp1_b32 s74, 10
	s_cbranch_scc0 .Lp8s_11
	v_mfma_f32_16x16x128_f8f6f4 v[116:119], v[0:7], v[216:223], v[116:119]
.Lp8s_11:
	s_bitcmp1_b32 s74, 6
	s_cbranch_scc0 .Lp8s_12
	v_mfma_f32_16x16x128_f8f6f4 v[132:135], v[0:7], v[208:215], v[132:135]
.Lp8s_12:
	s_bitcmp1_b32 s74, 7
	s_cbranch_scc0 .Lp8s_13
	v_mfma_f32_16x16x128_f8f6f4 v[128:131], v[8:15], v[208:215], v[128:131]
.Lp8s_13:
	s_bitcmp1_b32 s74, 3
	s_cbranch_scc0 .Lp8s_14
	v_mfma_f32_16x16x128_f8f6f4 v[144:147], v[8:15], v[180:187], v[144:147]

.Lp8s_16:
	s_bitcmp1_b32 s74, 17
	s_cbranch_scc0 .Lp8s_17
	v_mfma_f32_16x16x128_f8f6f4 v[88:91], v[24:31], v[208:215], v[88:91]
.Lp8s_17:
	s_bitcmp1_b32 s74, 21
	s_cbranch_scc0 .Lp8s_18
	v_mfma_f32_16x16x128_f8f6f4 v[72:75], v[24:31], v[216:223], v[72:75]
.Lp8s_18:
	s_bitcmp1_b32 s74, 20
	s_cbranch_scc0 .Lp8s_19
	v_mfma_f32_16x16x128_f8f6f4 v[76:79], v[16:23], v[216:223], v[76:79]
.Lp8s_19:
	s_bitcmp1_b32 s74, 24
	s_cbranch_scc0 .Lp8s_20
	v_mfma_f32_16x16x128_f8f6f4 v[60:63], v[16:23], v[224:231], v[60:63]
.Lp8s_20:
	s_bitcmp1_b32 s74, 25
	s_cbranch_scc0 .Lp8s_21
	v_mfma_f32_16x16x128_f8f6f4 v[56:59], v[24:31], v[224:231], v[56:59]
.Lp8s_21:
	s_bitcmp1_b32 s74, 29
	s_cbranch_scc0 .Lp8s_22
	v_mfma_f32_16x16x128_f8f6f4 v[40:43], v[24:31], v[232:239], v[40:43]
.Lp8s_22:
	s_bitcmp1_b32 s74, 28
	s_cbranch_scc0 .Lp8s_23
	v_mfma_f32_16x16x128_f8f6f4 v[44:47], v[16:23], v[232:239], v[44:47]
.Lp8s_23:
	s_setprio 0
	s_setprio 1
	s_bitcmp1_b32 s74, 30
	s_cbranch_scc0 .Lp8s_24
	v_mfma_f32_16x16x128_f8f6f4 v[36:39], v[0:7], v[232:239], v[36:39]
.Lp8s_24:
	s_bitcmp1_b32 s74, 31
	s_cbranch_scc0 .Lp8s_25
	v_mfma_f32_16x16x128_f8f6f4 v[32:35], v[8:15], v[232:239], v[32:35]
.Lp8s_25:
	s_bitcmp1_b32 s74, 27
	s_cbranch_scc0 .Lp8s_26
	v_mfma_f32_16x16x128_f8f6f4 v[48:51], v[8:15], v[224:231], v[48:51]
.Lp8s_26:
	s_bitcmp1_b32 s74, 26
	s_cbranch_scc0 .Lp8s_27
	v_mfma_f32_16x16x128_f8f6f4 v[52:55], v[0:7], v[224:231], v[52:55]
.Lp8s_27:
	s_bitcmp1_b32 s74, 22
	s_cbranch_scc0 .Lp8s_28
	v_mfma_f32_16x16x128_f8f6f4 v[68:71], v[0:7], v[216:223], v[68:71]
.Lp8s_28:
	s_bitcmp1_b32 s74, 23
	s_cbranch_scc0 .Lp8s_29
	v_mfma_f32_16x16x128_f8f6f4 v[64:67], v[8:15], v[216:223], v[64:67]
.Lp8s_29:
	s_bitcmp1_b32 s74, 19
	s_cbranch_scc0 .Lp8s_30
	v_mfma_f32_16x16x128_f8f6f4 v[80:83], v[8:15], v[208:215], v[80:83]

.Lp8s_32:
	s_bitcmp1_b32 s74, 1
	s_cbranch_scc0 .Lp8s_33
	v_mfma_f32_16x16x128_f8f6f4 v[152:155], v[8:15], v[208:215], v[152:155]
.Lp8s_33:
	s_bitcmp1_b32 s74, 5
	s_cbranch_scc0 .Lp8s_34
	v_mfma_f32_16x16x128_f8f6f4 v[136:139], v[8:15], v[216:223], v[136:139]
.Lp8s_34:
	s_bitcmp1_b32 s74, 4
	s_cbranch_scc0 .Lp8s_35
	v_mfma_f32_16x16x128_f8f6f4 v[140:143], v[0:7], v[216:223], v[140:143]
.Lp8s_35:
	s_bitcmp1_b32 s74, 8
	s_cbranch_scc0 .Lp8s_36
	v_mfma_f32_16x16x128_f8f6f4 v[124:127], v[0:7], v[224:231], v[124:127]
.Lp8s_36:
	s_bitcmp1_b32 s74, 9
	s_cbranch_scc0 .Lp8s_37
	v_mfma_f32_16x16x128_f8f6f4 v[120:123], v[8:15], v[224:231], v[120:123]
.Lp8s_37:
	s_bitcmp1_b32 s74, 13
	s_cbranch_scc0 .Lp8s_38
	v_mfma_f32_16x16x128_f8f6f4 v[104:107], v[8:15], v[232:239], v[104:107]
.Lp8s_38:
	s_bitcmp1_b32 s74, 12
	s_cbranch_scc0 .Lp8s_39
	v_mfma_f32_16x16x128_f8f6f4 v[108:111], v[0:7], v[232:239], v[108:111]
.Lp8s_39:
	s_setprio 0
	s_setprio 1
	s_bitcmp1_b32 s74, 14
	s_cbranch_scc0 .Lp8s_40
	v_mfma_f32_16x16x128_f8f6f4 v[100:103], v[16:23], v[232:239], v[100:103]
.Lp8s_40:
	s_bitcmp1_b32 s74, 15
	s_cbranch_scc0 .Lp8s_41
	v_mfma_f32_16x16x128_f8f6f4 v[96:99], v[24:31], v[232:239], v[96:99]
.Lp8s_41:
	s_bitcmp1_b32 s74, 11
	s_cbranch_scc0 .Lp8s_42
	v_mfma_f32_16x16x128_f8f6f4 v[112:115], v[24:31], v[224:231], v[112:115]
.Lp8s_42:
	s_bitcmp1_b32 s74, 10
	s_cbranch_scc0 .Lp8s_43
	v_mfma_f32_16x16x128_f8f6f4 v[116:119], v[16:23], v[224:231], v[116:119]
.Lp8s_43:
	s_bitcmp1_b32 s74, 6
	s_cbranch_scc0 .Lp8s_44
	v_mfma_f32_16x16x128_f8f6f4 v[132:135], v[16:23], v[216:223], v[132:135]
.Lp8s_44:
	s_bitcmp1_b32 s74, 7
	s_cbranch_scc0 .Lp8s_45
	v_mfma_f32_16x16x128_f8f6f4 v[128:131], v[24:31], v[216:223], v[128:131]
.Lp8s_45:
	s_bitcmp1_b32 s74, 3
	s_cbranch_scc0 .Lp8s_46
	v_mfma_f32_16x16x128_f8f6f4 v[144:147], v[24:31], v[208:215], v[144:147]

.Lp8s_48:
	s_bitcmp1_b32 s74, 17
	s_cbranch_scc0 .Lp8s_49
	v_mfma_f32_16x16x128_f8f6f4 v[88:91], v[8:15], v[208:215], v[88:91]
.Lp8s_49:
	s_bitcmp1_b32 s74, 21
	s_cbranch_scc0 .Lp8s_50
	v_mfma_f32_16x16x128_f8f6f4 v[72:75], v[8:15], v[216:223], v[72:75]
.Lp8s_50:
	s_bitcmp1_b32 s74, 20
	s_cbranch_scc0 .Lp8s_51
	v_mfma_f32_16x16x128_f8f6f4 v[76:79], v[0:7], v[216:223], v[76:79]
.Lp8s_51:
	s_bitcmp1_b32 s74, 24
	s_cbranch_scc0 .Lp8s_52
	v_mfma_f32_16x16x128_f8f6f4 v[60:63], v[0:7], v[224:231], v[60:63]
.Lp8s_52:
	s_bitcmp1_b32 s74, 25
	s_cbranch_scc0 .Lp8s_53
	v_mfma_f32_16x16x128_f8f6f4 v[56:59], v[8:15], v[224:231], v[56:59]
.Lp8s_53:
	s_bitcmp1_b32 s74, 29
	s_cbranch_scc0 .Lp8s_54
	v_mfma_f32_16x16x128_f8f6f4 v[40:43], v[8:15], v[232:239], v[40:43]
.Lp8s_54:
	s_bitcmp1_b32 s74, 28
	s_cbranch_scc0 .Lp8s_55
	v_mfma_f32_16x16x128_f8f6f4 v[44:47], v[0:7], v[232:239], v[44:47]
.Lp8s_55:
	s_setprio 0
	s_setprio 1
	s_bitcmp1_b32 s74, 30
	s_cbranch_scc0 .Lp8s_56
	v_mfma_f32_16x16x128_f8f6f4 v[36:39], v[16:23], v[232:239], v[36:39]
.Lp8s_56:
	s_bitcmp1_b32 s74, 31
	s_cbranch_scc0 .Lp8s_57
	v_mfma_f32_16x16x128_f8f6f4 v[32:35], v[24:31], v[232:239], v[32:35]
.Lp8s_57:
	s_bitcmp1_b32 s74, 27
	s_cbranch_scc0 .Lp8s_58
	v_mfma_f32_16x16x128_f8f6f4 v[48:51], v[24:31], v[224:231], v[48:51]
.Lp8s_58:
	s_bitcmp1_b32 s74, 26
	s_cbranch_scc0 .Lp8s_59
	v_mfma_f32_16x16x128_f8f6f4 v[52:55], v[16:23], v[224:231], v[52:55]
.Lp8s_59:
	s_bitcmp1_b32 s74, 22
	s_cbranch_scc0 .Lp8s_60
	v_mfma_f32_16x16x128_f8f6f4 v[68:71], v[16:23], v[216:223], v[68:71]
.Lp8s_60:
	s_bitcmp1_b32 s74, 23
	s_cbranch_scc0 .Lp8s_61
	v_mfma_f32_16x16x128_f8f6f4 v[64:67], v[24:31], v[216:223], v[64:67]
.Lp8s_61:
	s_bitcmp1_b32 s74, 19
	s_cbranch_scc0 .Lp8s_62
	v_mfma_f32_16x16x128_f8f6f4 v[80:83], v[24:31], v[208:215], v[80:83]

.LBB0_1358:
	s_add_u32 s30, s26, 0x1000
	s_addc_u32 s31, s27, 0
	s_mov_b32 m0, s49
	s_nop 0
	global_load_lds_dwordx4 v160, s[30:31]
	s_mov_b32 m0, s50
	s_nop 0
	global_load_lds_dwordx4 v164, s[30:31]
	ds_read_b128 v[16:19], v207
	ds_read_b128 v[20:23], v208
	ds_read_b128 v[24:27], v209
	ds_read_b128 v[28:31], v210
	ds_read_b128 v[0:3], v211
	ds_read_b128 v[4:7], v212
	ds_read_b128 v[8:11], v213
	ds_read_b128 v[12:15], v214
	s_add_u32 s28, s26, 0x10000
	s_addc_u32 s29, s27, 0
	s_cmpk_eq_i32 s59, 0x7c
	s_cselect_b32 s36, s55, s28
	s_cselect_b32 s37, s19, s29
	s_cselect_b32 s34, s56, s57
	s_cselect_b32 s35, s17, s58
	s_add_i32 m0, s25, 0xc000
	ds_read_b128 v[176:179], v224
	ds_read_b128 v[180:183], v224 offset:1024
	ds_read_b128 v[184:187], v224 offset:2048
	ds_read_b128 v[188:191], v224 offset:3072
	ds_read_b128 v[192:195], v224 offset:4096
	ds_read_b128 v[196:199], v224 offset:5120
	ds_read_b128 v[226:229], v224 offset:6144
	ds_read_b128 v[230:233], v224 offset:7168
	global_load_lds_dwordx4 v168, s[26:27]
	s_add_i32 m0, s25, 0xe000
	s_nop 0
	global_load_lds_dwordx4 v170, s[26:27]
	s_waitcnt vmcnt(8)
	s_waitcnt lgkmcnt(0)
	s_barrier
	s_setprio 1
	s_waitcnt lgkmcnt(0)
	v_mfma_f32_16x16x128_f8f6f4 v[156:159], v[16:23], v[176:183], v[156:159]
	v_mfma_f32_16x16x128_f8f6f4 v[152:155], v[24:31], v[176:183], v[152:155]
	v_mfma_f32_16x16x128_f8f6f4 v[136:139], v[24:31], v[184:191], v[136:139]
	v_mfma_f32_16x16x128_f8f6f4 v[144:147], v[16:23], v[184:191], v[144:147]
	v_mfma_f32_16x16x128_f8f6f4 v[124:127], v[16:23], v[192:199], v[124:127]
	v_mfma_f32_16x16x128_f8f6f4 v[120:123], v[24:31], v[192:199], v[120:123]
	v_mfma_f32_16x16x128_f8f6f4 v[104:107], v[24:31], v[226:233], v[104:107]
	v_mfma_f32_16x16x128_f8f6f4 v[112:115], v[16:23], v[226:233], v[112:115]
	s_setprio 0
	s_setprio 1
	v_mfma_f32_16x16x128_f8f6f4 v[100:103], v[0:7], v[226:233], v[100:103]
	v_mfma_f32_16x16x128_f8f6f4 v[96:99], v[8:15], v[226:233], v[96:99]
	v_mfma_f32_16x16x128_f8f6f4 v[108:111], v[8:15], v[192:199], v[108:111]
	v_mfma_f32_16x16x128_f8f6f4 v[116:119], v[0:7], v[192:199], v[116:119]
	v_mfma_f32_16x16x128_f8f6f4 v[132:135], v[0:7], v[184:191], v[132:135]
	v_mfma_f32_16x16x128_f8f6f4 v[128:131], v[8:15], v[184:191], v[128:131]
	v_mfma_f32_16x16x128_f8f6f4 v[140:143], v[8:15], v[176:183], v[140:143]
	v_mfma_f32_16x16x128_f8f6f4 v[148:151], v[0:7], v[176:183], v[148:151]
	s_setprio 0
	s_barrier
	s_mov_b32 m0, s33
	v_lshl_add_u64 v[176:177], s[34:35], 0, v[162:163]
	s_add_u32 s26, s34, 0x200000
	ds_read_b128 v[180:183], v224 offset:16384
	ds_read_b128 v[184:187], v224 offset:17408
	ds_read_b128 v[188:191], v224 offset:18432
	ds_read_b128 v[192:195], v224 offset:19456
	ds_read_b128 v[196:199], v224 offset:20480
	ds_read_b128 v[200:203], v224 offset:21504
	ds_read_b128 v[226:229], v224 offset:22528
	ds_read_b128 v[230:233], v224 offset:23552
	global_load_lds_dwordx4 v[176:177], off
	v_lshl_add_u64 v[178:179], s[34:35], 0, v[166:167]
	s_mov_b32 m0, s38
	s_addc_u32 s27, s35, 0
	global_load_lds_dwordx4 v[178:179], off
	s_mov_b32 m0, s39
	s_nop 0
	global_load_lds_dwordx4 v162, s[26:27]
	s_mov_b32 m0, s40
	s_nop 0
	global_load_lds_dwordx4 v166, s[26:27]
	s_waitcnt vmcnt(6)
	s_waitcnt lgkmcnt(0)
	s_barrier
	s_setprio 1
	s_waitcnt lgkmcnt(0)
	v_mfma_f32_16x16x128_f8f6f4 v[92:95], v[16:23], v[180:187], v[92:95]
	v_mfma_f32_16x16x128_f8f6f4 v[88:91], v[24:31], v[180:187], v[88:91]
	v_mfma_f32_16x16x128_f8f6f4 v[72:75], v[24:31], v[188:195], v[72:75]
	v_mfma_f32_16x16x128_f8f6f4 v[80:83], v[16:23], v[188:195], v[80:83]
	v_mfma_f32_16x16x128_f8f6f4 v[64:67], v[16:23], v[196:203], v[64:67]
	v_mfma_f32_16x16x128_f8f6f4 v[56:59], v[24:31], v[196:203], v[56:59]
	v_mfma_f32_16x16x128_f8f6f4 v[40:43], v[24:31], v[226:233], v[40:43]
	v_mfma_f32_16x16x128_f8f6f4 v[48:51], v[16:23], v[226:233], v[48:51]
	s_setprio 0
	s_setprio 1
	v_mfma_f32_16x16x128_f8f6f4 v[36:39], v[0:7], v[226:233], v[36:39]
	v_mfma_f32_16x16x128_f8f6f4 v[32:35], v[8:15], v[226:233], v[32:35]
	v_mfma_f32_16x16x128_f8f6f4 v[44:47], v[8:15], v[196:203], v[44:47]
	v_mfma_f32_16x16x128_f8f6f4 v[52:55], v[0:7], v[196:203], v[52:55]
	v_mfma_f32_16x16x128_f8f6f4 v[68:71], v[0:7], v[188:195], v[68:71]
	v_mfma_f32_16x16x128_f8f6f4 v[60:63], v[8:15], v[188:195], v[60:63]
	v_mfma_f32_16x16x128_f8f6f4 v[76:79], v[8:15], v[180:187], v[76:79]
	v_mfma_f32_16x16x128_f8f6f4 v[84:87], v[0:7], v[180:187], v[84:87]
	s_setprio 0
	s_barrier
	s_mov_b32 m0, s25
	s_nop 0
	global_load_lds_dwordx4 v160, s[36:37]
	s_mov_b32 m0, s41
	s_nop 0
	global_load_lds_dwordx4 v164, s[36:37]
	ds_read_b128 v[0:3], v215
	ds_read_b128 v[4:7], v216
	ds_read_b128 v[8:11], v217
	ds_read_b128 v[12:15], v218
	ds_read_b128 v[16:19], v219
	ds_read_b128 v[20:23], v220
	ds_read_b128 v[24:27], v221
	ds_read_b128 v[28:31], v222
	s_add_u32 s26, s36, 0x8000
	s_addc_u32 s27, s37, 0
	s_mov_b32 m0, s42
	ds_read_b128 v[180:183], v224 offset:32768
	ds_read_b128 v[184:187], v224 offset:33792
	ds_read_b128 v[188:191], v224 offset:34816
	ds_read_b128 v[192:195], v224 offset:35840
	ds_read_b128 v[196:199], v224 offset:36864
	ds_read_b128 v[200:203], v224 offset:37888
	ds_read_b128 v[226:229], v224 offset:38912
	ds_read_b128 v[230:233], v224 offset:39936
	global_load_lds_dwordx4 v160, s[26:27]
	s_mov_b32 m0, s43
	s_nop 0
	global_load_lds_dwordx4 v164, s[26:27]
	s_waitcnt vmcnt(8)
	s_waitcnt lgkmcnt(0)
	s_barrier
	s_setprio 1
	s_waitcnt lgkmcnt(0)
	v_mfma_f32_16x16x128_f8f6f4 v[156:159], v[0:7], v[180:187], v[156:159]
	v_mfma_f32_16x16x128_f8f6f4 v[152:155], v[8:15], v[180:187], v[152:155]
	v_mfma_f32_16x16x128_f8f6f4 v[136:139], v[8:15], v[188:195], v[136:139]
	v_mfma_f32_16x16x128_f8f6f4 v[144:147], v[0:7], v[188:195], v[144:147]
	v_mfma_f32_16x16x128_f8f6f4 v[124:127], v[0:7], v[196:203], v[124:127]
	v_mfma_f32_16x16x128_f8f6f4 v[120:123], v[8:15], v[196:203], v[120:123]
	v_mfma_f32_16x16x128_f8f6f4 v[104:107], v[8:15], v[226:233], v[104:107]
	v_mfma_f32_16x16x128_f8f6f4 v[112:115], v[0:7], v[226:233], v[112:115]
	s_setprio 0
	s_setprio 1
	v_mfma_f32_16x16x128_f8f6f4 v[100:103], v[16:23], v[226:233], v[100:103]
	v_mfma_f32_16x16x128_f8f6f4 v[96:99], v[24:31], v[226:233], v[96:99]
	v_mfma_f32_16x16x128_f8f6f4 v[108:111], v[24:31], v[196:203], v[108:111]
	v_mfma_f32_16x16x128_f8f6f4 v[116:119], v[16:23], v[196:203], v[116:119]
	v_mfma_f32_16x16x128_f8f6f4 v[132:135], v[16:23], v[188:195], v[132:135]
	v_mfma_f32_16x16x128_f8f6f4 v[128:131], v[24:31], v[188:195], v[128:131]
	v_mfma_f32_16x16x128_f8f6f4 v[140:143], v[24:31], v[180:187], v[140:143]
	v_mfma_f32_16x16x128_f8f6f4 v[148:151], v[16:23], v[180:187], v[148:151]
	s_setprio 0
	s_barrier
	s_mov_b32 m0, s47
	v_lshl_add_u64 v[176:177], v[176:177], 0, s[10:11]
	s_add_u32 s26, s34, 0x200080
	ds_read_b128 v[180:183], v224 offset:49152
	ds_read_b128 v[184:187], v224 offset:50176
	ds_read_b128 v[188:191], v224 offset:51200
	ds_read_b128 v[192:195], v224 offset:52224
	ds_read_b128 v[196:199], v224 offset:53248
	ds_read_b128 v[200:203], v224 offset:54272
	ds_read_b128 v[226:229], v224 offset:55296
	ds_read_b128 v[230:233], v224 offset:56320
	global_load_lds_dwordx4 v[176:177], off
	v_lshl_add_u64 v[176:177], v[178:179], 0, s[10:11]
	s_mov_b32 m0, s48
	s_addc_u32 s27, s35, 0
	global_load_lds_dwordx4 v[176:177], off
	s_mov_b32 m0, s51
	s_nop 0
	global_load_lds_dwordx4 v162, s[26:27]
	s_mov_b32 m0, s52
	s_nop 0
	global_load_lds_dwordx4 v166, s[26:27]
	s_waitcnt vmcnt(6)
	s_waitcnt lgkmcnt(0)
	s_barrier
	s_setprio 1
	s_waitcnt lgkmcnt(0)
	v_mfma_f32_16x16x128_f8f6f4 v[92:95], v[0:7], v[180:187], v[92:95]
	v_mfma_f32_16x16x128_f8f6f4 v[88:91], v[8:15], v[180:187], v[88:91]
	v_mfma_f32_16x16x128_f8f6f4 v[72:75], v[8:15], v[188:195], v[72:75]
	v_mfma_f32_16x16x128_f8f6f4 v[80:83], v[0:7], v[188:195], v[80:83]
	v_mfma_f32_16x16x128_f8f6f4 v[64:67], v[0:7], v[196:203], v[64:67]
	v_mfma_f32_16x16x128_f8f6f4 v[56:59], v[8:15], v[196:203], v[56:59]
	v_mfma_f32_16x16x128_f8f6f4 v[40:43], v[8:15], v[226:233], v[40:43]
	v_mfma_f32_16x16x128_f8f6f4 v[48:51], v[0:7], v[226:233], v[48:51]
	s_setprio 0
	s_setprio 1
	v_mfma_f32_16x16x128_f8f6f4 v[36:39], v[16:23], v[226:233], v[36:39]
	v_mfma_f32_16x16x128_f8f6f4 v[32:35], v[24:31], v[226:233], v[32:35]
	v_mfma_f32_16x16x128_f8f6f4 v[44:47], v[24:31], v[196:203], v[44:47]
	v_mfma_f32_16x16x128_f8f6f4 v[52:55], v[16:23], v[196:203], v[52:55]
	v_mfma_f32_16x16x128_f8f6f4 v[68:71], v[16:23], v[188:195], v[68:71]
	v_mfma_f32_16x16x128_f8f6f4 v[60:63], v[24:31], v[188:195], v[60:63]
	v_mfma_f32_16x16x128_f8f6f4 v[76:79], v[24:31], v[180:187], v[76:79]
	v_mfma_f32_16x16x128_f8f6f4 v[84:87], v[16:23], v[180:187], v[84:87]
	s_setprio 0
	s_barrier
	s_add_i32 s59, s59, 2
	s_add_u32 s57, s57, 0x100
	s_addc_u32 s58, s58, 0
	s_cmpk_gt_u32 s59, 0x7d
	s_mov_b64 s[26:27], s[28:29]
	s_cbranch_scc0 .LBB0_1358
	s_nop 15
	s_nop 15
	s_and_b64 vcc, exec, s[12:13]
	s_cbranch_vccz .LBB0_1361
	s_barrier
